# router hand-off: one arrival atomic carrying the XCC id, L2 write-back only when a row panel spans XCDs
# speedup vs baseline: 1.0255x; 1.0255x over previous
.LBB0_1018:
	s_barrier
	s_waitcnt vmcnt(0)
	v_cmp_eq_u32_e32 vcc, 0, v0
	s_waitcnt lgkmcnt(0)
	s_barrier
	s_and_saveexec_b64 s[0:1], vcc
	s_cbranch_execz .LBB0_1035
	s_ashr_i32 s7, s6, 31
	s_lshl_b64 s[4:5], s[6:7], 2
	s_add_u32 s4, s48, s4
	s_addc_u32 s5, s49, s5
	s_add_u32 s4, s4, 0x10000
	s_addc_u32 s5, s5, 0
	v_readlane_b32 s8, v253, 36
	s_mul_i32 s9, s8, s8
	s_lshl_b32 s8, s8, 8
	s_lshl_b32 s9, s9, 16
	s_or_b32 s9, s9, s8
	s_or_b32 s9, s9, 1
	v_mov_b32_e32 v1, 0
	v_mov_b32_e32 v2, s9
	global_atomic_add v1, v2, s[4:5]
	buffer_inv sc1
	s_mov_b32 s10, 0
.Lph_0:
	global_load_dword v2, v1, s[4:5] sc1
	s_waitcnt vmcnt(0)
	v_and_b32_e32 v3, 0xff, v2
	v_cmp_gt_u32_e32 vcc, 4, v3
	s_cbranch_vccz .Lphd_0
	s_sleep 1
	s_add_u32 s10, s10, 1
	s_cmp_lt_u32 s10, 0x100000
	s_cbranch_scc1 .Lph_0
.Lphd_0:
	s_lshl_b32 s9, s9, 2
	v_cmp_eq_u32_e32 vcc, s9, v2
	s_cbranch_vccnz .Lphx_0
	buffer_wbl2 sc1
	s_waitcnt vmcnt(0)
	v_mov_b32_e32 v2, 1
	global_atomic_add v1, v2, s[4:5] offset:4
	s_mov_b32 s10, 0
.Lpg_0:
	global_load_dword v2, v1, s[4:5] offset:4 sc1
	s_waitcnt vmcnt(0)
	v_cmp_gt_u32_e32 vcc, 4, v2
	s_cbranch_vccz .Lpgd_0
	s_sleep 1
	s_add_u32 s10, s10, 1
	s_cmp_lt_u32 s10, 0x100000
	s_cbranch_scc1 .Lpg_0
.Lpgd_0:
	buffer_inv sc1
.Lphx_0:
	s_waitcnt vmcnt(0)
.LBB0_1035:
	s_or_b64 exec, exec, s[0:1]
	v_mov_b32_e32 v19, v0
	s_barrier
	v_readlane_b32 s52, v253, 18
	v_and_b32_e32 v21, 63, v19
	v_lshlrev_b32_e32 v22, 4, v21
	v_readlane_b32 s62, v253, 28
	v_readlane_b32 s63, v253, 29
	s_nop 4
	global_load_dwordx4 v[2:5], v22, s[62:63]
	global_load_dwordx4 v[6:9], v22, s[62:63] offset:1024
	global_load_dwordx4 v[10:13], v22, s[62:63] offset:2048
	global_load_dwordx4 v[14:17], v22, s[62:63] offset:3072
	v_lshrrev_b32_e32 v20, 2, v19
	v_and_b32_e32 v38, 12, v20
	v_mbcnt_lo_u32_b32 v20, -1, 0
	v_and_b32_e32 v18, 15, v19
	v_lshrrev_b32_e32 v24, 6, v19
	v_bfe_u32 v33, v19, 6, 1
	v_mbcnt_hi_u32_b32 v34, -1, v20
	v_and_b32_e32 v29, 0xffffff80, v19
	v_ashrrev_i32_e32 v1, 7, v19
	v_and_b32_e32 v26, 64, v34
	v_add_u32_e32 v29, 0, v29
	v_lshlrev_b32_e32 v31, 6, v33
	v_lshlrev_b32_e32 v32, 2, v18
	v_bitop3_b32 v24, v24, 1, v24 bitop3:0xc
	v_lshl_add_u32 v25, v1, 11, 0
	v_xor_b32_e32 v20, 16, v34
	v_add_u32_e32 v27, 64, v26
	v_lshlrev_b32_e32 v30, 10, v33
	v_add3_u32 v42, v29, v31, v32
	v_lshlrev_b32_e32 v31, 10, v24
	v_cmp_lt_i32_e32 vcc, v20, v27
	v_add3_u32 v41, v25, v30, v22
	v_add3_u32 v43, v25, v31, v22
	v_lshlrev_b32_e32 v22, 6, v24
	v_cndmask_b32_e32 v20, v34, v20, vcc
	v_add3_u32 v44, v29, v22, v32
	v_bfe_u32 v22, v19, 5, 1
	v_lshlrev_b32_e32 v39, 2, v20
	v_xor_b32_e32 v20, 32, v34
	v_cmp_eq_u32_e64 s[4:5], v22, v33
	v_or_b32_e32 v22, v26, v38
	v_cmp_lt_i32_e32 vcc, v20, v27
	v_lshlrev_b32_e32 v45, 2, v22
	v_xor_b32_e32 v22, 1, v34
	v_cndmask_b32_e32 v20, v34, v20, vcc
	v_cmp_lt_i32_e32 vcc, v22, v27
	v_mov_b32_e32 v23, 0
	v_readlane_b32 s8, v252, 9
	v_cndmask_b32_e32 v22, v34, v22, vcc
	v_lshlrev_b32_e32 v46, 2, v22
	v_xor_b32_e32 v22, 2, v34
	v_cmp_lt_i32_e32 vcc, v22, v27
	v_lshlrev_b32_e32 v40, 2, v20
	v_lshlrev_b32_e32 v20, 2, v21
	v_cndmask_b32_e32 v22, v34, v22, vcc
	v_lshlrev_b32_e32 v47, 2, v22
	v_xor_b32_e32 v22, 4, v34
	v_cmp_lt_i32_e32 vcc, v22, v27
	v_cmp_gt_u32_e64 s[0:1], 16, v21
	v_readlane_b32 s9, v252, 10
	v_cndmask_b32_e32 v22, v34, v22, vcc
	v_lshlrev_b32_e32 v48, 2, v22
	v_xor_b32_e32 v22, 8, v34
	v_cmp_lt_i32_e32 vcc, v22, v27
	v_lshlrev_b32_e32 v28, 12, v18
	s_add_i32 s10, s18, s6
	v_cndmask_b32_e32 v22, v34, v22, vcc
	v_lshlrev_b32_e32 v49, 2, v22
	v_lshlrev_b32_e32 v22, 3, v21
	v_mov_b32_e32 v21, v23
	v_lshl_add_u64 v[26:27], s[8:9], 0, v[20:21]
	v_lshlrev_b32_e32 v20, 11, v33
	v_and_b32_e32 v21, 48, v19
	v_lshl_add_u64 v[24:25], s[84:85], 0, v[22:23]
	v_or3_b32 v22, v28, v20, v21
	v_lshrrev_b32_e32 v19, 1, v19
	s_lshl_b32 s7, s18, 4
	s_lshl_b32 s6, s6, 4
	v_lshl_add_u64 v[20:21], s[48:49], 0, v[22:23]
	s_mov_b64 s[8:9], 0x300100
	v_and_or_b32 v22, v19, 24, v30
	v_add_u32_e32 v19, s10, v1
	s_add_i32 s7, s7, s6
	v_lshl_add_u64 v[28:29], v[20:21], 0, s[8:9]
	v_lshl_add_u64 v[20:21], s[48:49], 0, v[22:23]
	s_mov_b64 s[8:9], 0x800080
	v_lshl_or_b32 v32, v19, 4, v18
	v_lshl_add_u32 v19, v1, 4, s7
	v_lshl_add_u64 v[30:31], v[20:21], 0, s[8:9]
	v_lshl_or_b32 v22, v33, 3, v19
	v_lshlrev_b32_e32 v19, 2, v34
	v_lshlrev_b32_e32 v20, 5, v33
	s_movk_i32 s6, 0x100
	v_readlane_b32 s62, v252, 7
	v_or_b32_e32 v50, 4, v45
	v_or_b32_e32 v51, 8, v45
	v_or_b32_e32 v52, 12, v45
	v_and_or_b32 v53, v19, s6, v20
	s_mov_b64 s[6:7], 0x200
	v_mov_b32_e32 v54, 0x358637bd
	s_mov_b32 s11, 0x800000
	s_mov_b32 s12, 0x3fb8aa3b
	s_mov_b32 s13, 0xc2ce8ed0
	s_mov_b32 s14, 0x42b17218
	v_lshlrev_b32_e32 v55, 2, v18
	v_mov_b32_e32 v56, -1
	s_mov_b32 s15, 0xc3e00000
	v_mov_b32_e32 v57, 0x7f800000
	v_mov_b32_e32 v58, 0x43e00000
	v_readlane_b32 s63, v252, 8
	v_readlane_b32 s53, v253, 19
	v_readlane_b32 s54, v253, 20
	v_readlane_b32 s55, v253, 21
	v_readlane_b32 s56, v253, 22
	v_readlane_b32 s57, v253, 23
	v_readlane_b32 s58, v253, 24
	v_readlane_b32 s59, v253, 25
	v_readlane_b32 s60, v253, 26
	v_readlane_b32 s61, v253, 27
	v_readlane_b32 s64, v253, 30
	v_readlane_b32 s65, v253, 31
	v_readlane_b32 s66, v253, 32
	v_readlane_b32 s67, v253, 33

.LBB0_2298:
	s_barrier
	s_waitcnt vmcnt(0)
	v_cmp_eq_u32_e32 vcc, 0, v0
	s_waitcnt lgkmcnt(0)
	s_barrier
	s_and_saveexec_b64 s[0:1], vcc
	s_cbranch_execz .LBB0_2315
	s_ashr_i32 s7, s6, 31
	s_lshl_b64 s[4:5], s[6:7], 2
	v_readlane_b32 s10, v253, 34
	v_readlane_b32 s11, v253, 35
	s_add_u32 s4, s10, s4
	s_addc_u32 s5, s11, s5
	s_add_u32 s4, s4, 0xd000
	s_addc_u32 s5, s5, 0
	v_readlane_b32 s8, v253, 36
	s_mul_i32 s9, s8, s8
	s_lshl_b32 s8, s8, 8
	s_lshl_b32 s9, s9, 16
	s_or_b32 s9, s9, s8
	s_or_b32 s9, s9, 1
	v_mov_b32_e32 v1, 0
	v_mov_b32_e32 v2, s9
	global_atomic_add v1, v2, s[4:5]
	buffer_inv sc1
	s_mov_b32 s10, 0

.Lpgd_1:
	buffer_inv sc1
.Lphx_1:
	s_waitcnt vmcnt(0)
.LBB0_2315:
	s_or_b64 exec, exec, s[0:1]
	v_readlane_b32 s52, v253, 18
	v_readlane_b32 s62, v253, 28
	v_readlane_b32 s63, v253, 29
	v_mov_b32_e32 v19, v0
	s_barrier
	s_mov_b64 s[10:11], s[62:63]
	s_add_u32 s0, s10, 0x1000
	v_and_b32_e32 v21, 63, v19
	v_lshlrev_b32_e32 v22, 4, v21
	s_addc_u32 s1, s11, 0
	v_or_b32_e32 v10, 0x400, v22
	v_or_b32_e32 v18, 0x800, v22
	global_load_dwordx4 v[2:5], v22, s[0:1]
	global_load_dwordx4 v[6:9], v10, s[0:1]
	v_or_b32_e32 v20, 0xc00, v22
	global_load_dwordx4 v[10:13], v18, s[0:1]
	global_load_dwordx4 v[14:17], v20, s[0:1]
	v_lshrrev_b32_e32 v20, 2, v19
	v_and_b32_e32 v38, 12, v20
	v_mbcnt_lo_u32_b32 v20, -1, 0
	v_and_b32_e32 v18, 15, v19
	v_lshrrev_b32_e32 v24, 6, v19
	v_bfe_u32 v33, v19, 6, 1
	v_mbcnt_hi_u32_b32 v34, -1, v20
	v_and_b32_e32 v29, 0xffffff80, v19
	v_ashrrev_i32_e32 v1, 7, v19
	v_and_b32_e32 v26, 64, v34
	v_add_u32_e32 v29, 0, v29
	v_lshlrev_b32_e32 v31, 6, v33
	v_lshlrev_b32_e32 v32, 2, v18
	v_bitop3_b32 v24, v24, 1, v24 bitop3:0xc
	v_lshl_add_u32 v25, v1, 11, 0
	v_xor_b32_e32 v20, 16, v34
	v_add_u32_e32 v27, 64, v26
	v_lshlrev_b32_e32 v30, 10, v33
	v_add3_u32 v42, v29, v31, v32
	v_lshlrev_b32_e32 v31, 10, v24
	v_cmp_lt_i32_e32 vcc, v20, v27
	v_add3_u32 v41, v25, v30, v22
	v_add3_u32 v43, v25, v31, v22
	v_lshlrev_b32_e32 v22, 6, v24
	v_cndmask_b32_e32 v20, v34, v20, vcc
	v_add3_u32 v44, v29, v22, v32
	v_bfe_u32 v22, v19, 5, 1
	v_lshlrev_b32_e32 v39, 2, v20
	v_xor_b32_e32 v20, 32, v34
	v_cmp_eq_u32_e64 s[4:5], v22, v33
	v_or_b32_e32 v22, v26, v38
	v_cmp_lt_i32_e32 vcc, v20, v27
	v_lshlrev_b32_e32 v45, 2, v22
	v_xor_b32_e32 v22, 1, v34
	v_cndmask_b32_e32 v20, v34, v20, vcc
	v_cmp_lt_i32_e32 vcc, v22, v27
	v_mov_b32_e32 v23, 0
	v_lshlrev_b32_e32 v40, 2, v20
	v_cndmask_b32_e32 v22, v34, v22, vcc
	v_lshlrev_b32_e32 v46, 2, v22
	v_xor_b32_e32 v22, 2, v34
	v_cmp_lt_i32_e32 vcc, v22, v27
	v_lshlrev_b32_e32 v20, 2, v21
	v_cmp_gt_u32_e64 s[0:1], 16, v21
	v_cndmask_b32_e32 v22, v34, v22, vcc
	v_lshlrev_b32_e32 v47, 2, v22
	v_xor_b32_e32 v22, 4, v34
	v_cmp_lt_i32_e32 vcc, v22, v27
	v_lshlrev_b32_e32 v28, 12, v18
	s_add_i32 s10, s18, s6
	v_cndmask_b32_e32 v22, v34, v22, vcc
	v_lshlrev_b32_e32 v48, 2, v22
	v_xor_b32_e32 v22, 8, v34
	v_cmp_lt_i32_e32 vcc, v22, v27
	s_lshl_b32 s7, s18, 4
	s_lshl_b32 s6, s6, 4
	v_cndmask_b32_e32 v22, v34, v22, vcc
	v_lshlrev_b32_e32 v49, 2, v22
	v_lshlrev_b32_e32 v22, 3, v21
	v_mov_b32_e32 v21, v23
	v_lshl_add_u64 v[26:27], s[82:83], 0, v[20:21]
	v_lshlrev_b32_e32 v20, 11, v33
	v_and_b32_e32 v21, 48, v19
	v_lshl_add_u64 v[24:25], s[84:85], 0, v[22:23]
	v_or3_b32 v22, v28, v20, v21
	v_lshrrev_b32_e32 v19, 1, v19
	v_lshl_add_u64 v[20:21], s[48:49], 0, v[22:23]
	s_mov_b64 s[8:9], 0x310100
	v_and_or_b32 v22, v19, 24, v30
	v_add_u32_e32 v19, s10, v1
	s_add_i32 s7, s7, s6
	v_readlane_b32 s64, v253, 30
	v_readlane_b32 s65, v253, 31
	v_lshl_add_u64 v[28:29], v[20:21], 0, s[8:9]
	v_lshl_add_u64 v[20:21], s[48:49], 0, v[22:23]
	s_mov_b64 s[8:9], 0x800080
	v_lshl_or_b32 v32, v19, 4, v18
	v_lshl_add_u32 v19, v1, 4, s7
	v_lshl_add_u64 v[30:31], v[20:21], 0, s[8:9]
	v_lshl_or_b32 v22, v33, 3, v19
	v_lshlrev_b32_e32 v19, 2, v34
	v_lshlrev_b32_e32 v20, 5, v33
	s_movk_i32 s6, 0x100
	v_readlane_b32 s62, v252, 7
	v_readlane_b32 s64, v252, 20
	v_or_b32_e32 v50, 4, v45
	v_or_b32_e32 v51, 8, v45
	v_or_b32_e32 v52, 12, v45
	v_and_or_b32 v53, v19, s6, v20
	s_mov_b64 s[6:7], 0x200
	v_mov_b32_e32 v54, 0x358637bd
	s_mov_b32 s11, 0x800000
	s_mov_b32 s12, 0x3fb8aa3b
	s_mov_b32 s13, 0xc2ce8ed0
	s_mov_b32 s14, 0x42b17218
	v_lshlrev_b32_e32 v55, 2, v18
	v_mov_b32_e32 v56, -1
	s_mov_b32 s15, 0xc3e00000
	v_mov_b32_e32 v57, 0x7f800000
	v_mov_b32_e32 v58, 0x43e00000
	v_readlane_b32 s63, v252, 8
	v_readlane_b32 s65, v252, 21
	v_readlane_b32 s53, v253, 19
	v_readlane_b32 s54, v253, 20
	v_readlane_b32 s55, v253, 21
	v_readlane_b32 s56, v253, 22
	v_readlane_b32 s57, v253, 23
	v_readlane_b32 s58, v253, 24
	v_readlane_b32 s59, v253, 25
	v_readlane_b32 s60, v253, 26
	v_readlane_b32 s61, v253, 27
	v_readlane_b32 s66, v253, 32
	v_readlane_b32 s67, v253, 33
